# P0: the 512 absorbed-query-weight items (compute only) are dealt to workgroups 0..127 so that the other half starts the HBM-bound conversion queue at once
# speedup vs baseline: 1.0041x; 1.0041x over previous
; #define LAS __attribute__((address_space(3)))
; #define IN(k) ((const float*)gptr(ldp(PT, k)))
; __global__ void __launch_bounds__(NWAVES * 64, 2) fwd(Args args) {
;     ...
;         const float* w_in = IN(4);
;         { LAS float* wt = (LAS float*)F.lds; LAS float* uk = wt + 64 * 65;
;           for (int it = F.bx; it < NL * 8 * 16; it += F.G) { const int l = it >> 7, h = (it >> 4) & 7, kb = it & 15;
;             const float* Wl = w_in + (size_t)l * D * DIN + (size_t)(kb * 64) * DIN + h * 64; const float* wuk = IN(6) + (size_t)l * 128 * 512 + h * 64;
;             { float t8[8], u16[16];
; #pragma unroll
;               for (int j = 0; j < 8; ++j) { const int i = F.tid + 512 * j; t8[j] = Wl[(size_t)(i >> 6) * DIN + (i & 63)]; }
; #pragma unroll
;               for (int j = 0; j < 16; ++j) { const int i = F.tid + 512 * j; u16[j] = wuk[(size_t)(i >> 6) * 512 + (i & 63)]; }
; #pragma unroll
;               for (int j = 0; j < 8; ++j) { const int i = F.tid + 512 * j; wt[(i >> 6) * 65 + (i & 63)] = t8[j]; }
; #pragma unroll
;               for (int j = 0; j < 16; ++j) { const int i = F.tid + 512 * j; uk[(i >> 6) * 65 + (i & 63)] = u16[j]; } }
.LBB0_12:
	s_or_b64 exec, exec, s[2:3]
	s_load_dwordx2 s[92:93], s[0:1], 0x118
	s_and_b32 s94, s8, 0xffffffc0
	v_writelane_b32 v255, s91, 2
	s_mov_b32 s0, 0
	v_mbcnt_lo_u32_b32 v142, -1, 0
	s_waitcnt lgkmcnt(0)
	s_cmp_lt_i32 s92, 1
	s_cselect_b64 s[2:3], -1, 0
	s_cmp_gt_i32 s93, 0
	s_cselect_b64 s[4:5], -1, 0
	v_writelane_b32 v255, s92, 3
	s_and_b64 s[2:3], s[2:3], s[4:5]
	s_andn2_b64 vcc, exec, s[2:3]
	v_writelane_b32 v255, s93, 4
	v_writelane_b32 v255, s94, 5
	s_barrier
	s_cbranch_vccnz .LBB0_309
	s_add_i32 s52, s0, 0
	s_add_i32 s0, s52, 0x20450
	v_mbcnt_hi_u32_b32 v80, -1, v142
	v_mov_b32_e32 v0, s0
	v_mov_b32_e32 v2, v80
	ds_read_b64 v[0:1], v0
	s_add_i32 s0, s52, 0x2016c
	v_add_u32_e32 v64, s94, v2
	v_mov_b32_e32 v2, s0
	ds_read_b32 v2, v2
	s_waitcnt lgkmcnt(1)
	v_readfirstlane_b32 s58, v0
	v_readfirstlane_b32 s59, v1
	v_mov_b32_e32 v0, s97
	s_add_u32 s64, s58, 0x100000
	s_waitcnt lgkmcnt(0)
	v_subrev_co_u32_e32 v1, vcc, 1, v2
	s_addc_u32 s65, s59, 0
	s_nop 0
	v_cndmask_b32_e32 v0, v1, v0, vcc
	s_add_i32 s0, s52, 0x20448
	v_readfirstlane_b32 s62, v0
	s_mov_b32 s60, s91
	v_mov_b32_e32 v0, s0
	ds_read_b64 v[0:1], v0
	s_add_i32 s0, s52, 0x20360
	s_waitcnt lgkmcnt(0)
	v_mov_b32_e32 v0, s0
	ds_read_b64 v[2:3], v0
	v_and_b32_e32 v81, 63, v64
	v_readfirstlane_b32 s79, v64
	s_cmpk_gt_i32 s62, 0x7f
	v_mov_b32_e32 v1, 0
	s_waitcnt lgkmcnt(0)
	v_readfirstlane_b32 s53, v3
	v_readfirstlane_b32 s54, v2
	v_lshlrev_b32_e32 v72, 4, v64
	s_cbranch_scc1 .LBB0_18
	v_add_u32_e32 v6, 0x200, v64
	v_ashrrev_i32_e32 v12, 6, v6
	v_add_u32_e32 v6, 0x400, v64
	v_ashrrev_i32_e32 v16, 6, v6
	v_add_u32_e32 v6, 0x600, v64
	v_ashrrev_i32_e32 v20, 6, v6
	v_add_u32_e32 v6, 0x800, v64
	v_ashrrev_i32_e32 v24, 6, v6
	v_add_u32_e32 v6, 0xa00, v64
	v_ashrrev_i32_e32 v28, 6, v6
	v_add_u32_e32 v6, 0xc00, v64
	v_ashrrev_i32_e32 v32, 6, v6
	v_add_u32_e32 v6, 0xe00, v64
	v_ashrrev_i32_e32 v36, 6, v6
	v_add_u32_e32 v6, 0x1000, v64
	v_ashrrev_i32_e32 v38, 6, v6
	v_add_u32_e32 v6, 0x1200, v64
	v_ashrrev_i32_e32 v40, 6, v6
	v_add_u32_e32 v6, 0x1400, v64
	v_ashrrev_i32_e32 v42, 6, v6
	v_add_u32_e32 v6, 0x1600, v64
	v_ashrrev_i32_e32 v44, 6, v6
	v_add_u32_e32 v6, 0x1800, v64
	v_ashrrev_i32_e32 v46, 6, v6
	v_add_u32_e32 v6, 0x1a00, v64
	v_ashrrev_i32_e32 v48, 6, v6
	v_add_u32_e32 v6, 0x1c00, v64
	v_ashrrev_i32_e32 v50, 6, v6
	v_add_u32_e32 v6, 0x1e00, v64
	s_movk_i32 s0, 0x104
	v_ashrrev_i32_e32 v8, 6, v64
	v_ashrrev_i32_e32 v52, 6, v6
	v_lshl_add_u32 v0, v81, 2, s52
	v_mul_lo_u32 v6, v8, s0
	v_mul_lo_u32 v7, v12, s0
	v_mul_lo_u32 v10, v16, s0
	v_mul_lo_u32 v11, v20, s0
	v_mul_lo_u32 v13, v24, s0
	v_mul_lo_u32 v14, v28, s0
	v_mul_lo_u32 v15, v32, s0
	v_mul_lo_u32 v17, v36, s0
	v_mul_lo_u32 v18, v38, s0
	v_mul_lo_u32 v19, v40, s0
	v_mul_lo_u32 v21, v42, s0
	v_mul_lo_u32 v22, v44, s0
	v_mul_lo_u32 v23, v46, s0
	v_mul_lo_u32 v25, v48, s0
	v_mul_lo_u32 v26, v50, s0
	v_mul_lo_u32 v27, v52, s0
	v_ashrrev_i32_e32 v2, 2, v64
	v_and_b32_e32 v4, 48, v72
	v_add_u32_e32 v65, v0, v6
	v_add_u32_e32 v73, v0, v7
	v_add_u32_e32 v74, v0, v10
	v_add_u32_e32 v75, v0, v11
	v_add_u32_e32 v76, v0, v13
	v_add_u32_e32 v77, v0, v14
	v_add_u32_e32 v78, v0, v15
	v_add_u32_e32 v79, v0, v17
	v_add_u32_e32 v82, v0, v18
	v_add_u32_e32 v83, v0, v19
	v_add_u32_e32 v84, v0, v21
	v_add_u32_e32 v85, v0, v22
	v_add_u32_e32 v86, v0, v23
	v_add_u32_e32 v87, v0, v25
	v_add_u32_e32 v88, v0, v26
	v_add_u32_e32 v89, v0, v27
	v_mov_b32_e32 v0, s52
	v_mad_u32_u24 v90, v4, s0, v0
	v_mul_lo_u32 v0, v2, s0
	v_ashrrev_i32_e32 v9, 31, v8
	s_movk_i32 s1, 0x76a0
	v_ashrrev_i32_e32 v13, 31, v12
	v_ashrrev_i32_e32 v17, 31, v16
	v_ashrrev_i32_e32 v21, 31, v20
	v_ashrrev_i32_e32 v25, 31, v24
	v_ashrrev_i32_e32 v29, 31, v28
	v_ashrrev_i32_e32 v33, 31, v32
	v_ashrrev_i32_e32 v37, 31, v36
	v_ashrrev_i32_e32 v39, 31, v38
	v_ashrrev_i32_e32 v41, 31, v40
	v_ashrrev_i32_e32 v43, 31, v42
	v_ashrrev_i32_e32 v45, 31, v44
	v_ashrrev_i32_e32 v47, 31, v46
	v_ashrrev_i32_e32 v49, 31, v48
	v_ashrrev_i32_e32 v51, 31, v50
	v_ashrrev_i32_e32 v53, 31, v52
	v_add_u32_e32 v0, s52, v0
	s_add_i32 s4, s52, 0x20370
	v_ashrrev_i32_e32 v3, 31, v2
	v_mov_b32_e32 v5, v1
	v_mad_i64_i32 v[6:7], s[2:3], v8, s1, 0
	v_lshlrev_b64 v[8:9], 11, v[8:9]
	v_mad_i64_i32 v[10:11], s[2:3], v12, s1, 0
	v_lshlrev_b64 v[12:13], 11, v[12:13]
	v_mad_i64_i32 v[14:15], s[2:3], v16, s1, 0
	v_lshlrev_b64 v[16:17], 11, v[16:17]
	v_mad_i64_i32 v[18:19], s[2:3], v20, s1, 0
	v_lshlrev_b64 v[20:21], 11, v[20:21]
	v_mad_i64_i32 v[22:23], s[2:3], v24, s1, 0
	v_lshlrev_b64 v[24:25], 11, v[24:25]
	v_mad_i64_i32 v[26:27], s[2:3], v28, s1, 0
	v_lshlrev_b64 v[28:29], 11, v[28:29]
	v_mad_i64_i32 v[30:31], s[2:3], v32, s1, 0
	v_lshlrev_b64 v[32:33], 11, v[32:33]
	v_mad_i64_i32 v[34:35], s[2:3], v36, s1, 0
	v_lshlrev_b64 v[36:37], 11, v[36:37]
	v_lshlrev_b64 v[38:39], 11, v[38:39]
	v_lshlrev_b64 v[40:41], 11, v[40:41]
	v_lshlrev_b64 v[42:43], 11, v[42:43]
	v_lshlrev_b64 v[44:45], 11, v[44:45]
	v_lshlrev_b64 v[46:47], 11, v[46:47]
	v_lshlrev_b64 v[48:49], 11, v[48:49]
	v_lshlrev_b64 v[50:51], 11, v[50:51]
	v_lshlrev_b64 v[52:53], 11, v[52:53]
	s_mov_b32 s1, 0
	v_add_u32_e32 v91, 0x4100, v0
	s_mov_b32 s5, 0xc2fe0000
	s_mov_b32 s6, 0x40c0c00
	s_mov_b32 s7, s62
	v_mov_b32_e32 v92, 0x42fe0000

; __global__ void __launch_bounds__(NWAVES * 64, 2) fwd(Args args) {
;     ...
;             for (int d = 0; d < 64; ++d) { const float wv = uk[c * 65 + d];
; #pragma unroll
;                 for (int j = 0; j < 16; ++j) a[j] += wv * wt[(kq * 16 + j) * 65 + d]; }
.LBB0_16:
	v_add_u32_e32 v0, s9, v91
	v_add_u32_e32 v93, s9, v90
	ds_read2_b32 v[94:95], v0 offset1:1
	ds_read2_b32 v[96:97], v93 offset1:1
	ds_read2_b32 v[98:99], v93 offset0:65 offset1:66
	s_add_i32 s9, s9, 16
	s_cmpk_eq_i32 s9, 0x100
	s_waitcnt lgkmcnt(1)
	v_mov_b32_e32 v100, v96
	s_waitcnt lgkmcnt(0)
	v_mov_b32_e32 v101, v98
	v_pk_fma_f32 v[70:71], v[94:95], v[100:101], v[70:71] op_sel_hi:[0,1,1]
	ds_read2_b32 v[100:101], v93 offset0:130 offset1:131
	ds_read2_b32 v[102:103], v93 offset0:195 offset1:196
	v_add_u32_e32 v96, 0x410, v93
	v_mov_b32_e32 v98, v97
	v_pk_fma_f32 v[70:71], v[94:95], v[98:99], v[70:71] op_sel:[1,0,0]
	s_waitcnt lgkmcnt(1)
	v_mov_b32_e32 v104, v100
	s_waitcnt lgkmcnt(0)
	v_mov_b32_e32 v105, v102
	v_pk_fma_f32 v[68:69], v[94:95], v[104:105], v[68:69] op_sel_hi:[0,1,1]
	ds_read2_b32 v[104:105], v96 offset1:1
	v_add_u32_e32 v96, 0x514, v93
	ds_read2_b32 v[106:107], v96 offset1:1
	v_add_u32_e32 v96, 0x618, v93
	v_mov_b32_e32 v102, v101
	s_waitcnt lgkmcnt(1)
	v_mov_b32_e32 v108, v104
	v_pk_fma_f32 v[68:69], v[94:95], v[102:103], v[68:69] op_sel:[1,0,0]
	s_waitcnt lgkmcnt(0)
	v_mov_b32_e32 v109, v106
	v_pk_fma_f32 v[66:67], v[94:95], v[108:109], v[66:67] op_sel_hi:[0,1,1]
	ds_read2_b32 v[108:109], v96 offset1:1
	v_add_u32_e32 v96, 0x71c, v93
	ds_read2_b32 v[110:111], v96 offset1:1
	v_add_u32_e32 v96, 0x820, v93
	v_mov_b32_e32 v106, v105
	s_waitcnt lgkmcnt(1)
	v_mov_b32_e32 v112, v108
	v_pk_fma_f32 v[66:67], v[94:95], v[106:107], v[66:67] op_sel:[1,0,0]
	s_waitcnt lgkmcnt(0)
	v_mov_b32_e32 v113, v110
	v_pk_fma_f32 v[62:63], v[94:95], v[112:113], v[62:63] op_sel_hi:[0,1,1]
	ds_read2_b32 v[112:113], v96 offset1:1
	v_add_u32_e32 v96, 0x924, v93
	ds_read2_b32 v[114:115], v96 offset1:1
	v_add_u32_e32 v96, 0xa28, v93
	v_mov_b32_e32 v110, v109
	s_waitcnt lgkmcnt(1)
	v_mov_b32_e32 v116, v112
	v_pk_fma_f32 v[62:63], v[94:95], v[110:111], v[62:63] op_sel:[1,0,0]
	s_waitcnt lgkmcnt(0)
	v_mov_b32_e32 v117, v114
	v_pk_fma_f32 v[60:61], v[94:95], v[116:117], v[60:61] op_sel_hi:[0,1,1]
	ds_read2_b32 v[116:117], v96 offset1:1
	v_add_u32_e32 v96, 0xb2c, v93
	ds_read2_b32 v[118:119], v96 offset1:1
	v_add_u32_e32 v96, 0xc30, v93
	v_mov_b32_e32 v114, v113
	s_waitcnt lgkmcnt(1)
	v_mov_b32_e32 v120, v116
	v_pk_fma_f32 v[60:61], v[94:95], v[114:115], v[60:61] op_sel:[1,0,0]
	s_waitcnt lgkmcnt(0)
	v_mov_b32_e32 v121, v118
	v_pk_fma_f32 v[58:59], v[94:95], v[120:121], v[58:59] op_sel_hi:[0,1,1]
	ds_read2_b32 v[120:121], v96 offset1:1
	v_add_u32_e32 v96, 0xd34, v93
	ds_read2_b32 v[122:123], v96 offset1:1
	v_add_u32_e32 v96, 0xe38, v93
	v_mov_b32_e32 v118, v117
	s_waitcnt lgkmcnt(1)
	v_mov_b32_e32 v124, v120
	v_pk_fma_f32 v[58:59], v[94:95], v[118:119], v[58:59] op_sel:[1,0,0]
	s_waitcnt lgkmcnt(0)
	v_mov_b32_e32 v125, v122
	v_pk_fma_f32 v[56:57], v[94:95], v[124:125], v[56:57] op_sel_hi:[0,1,1]
	ds_read2_b32 v[124:125], v96 offset1:1
	v_add_u32_e32 v96, 0xf3c, v93
	ds_read2_b32 v[126:127], v96 offset1:1
	v_mov_b32_e32 v122, v121
	v_pk_fma_f32 v[56:57], v[94:95], v[122:123], v[56:57] op_sel:[1,0,0]
	s_waitcnt lgkmcnt(1)
	v_mov_b32_e32 v128, v124
	s_waitcnt lgkmcnt(0)
	v_mov_b32_e32 v129, v126
	v_pk_fma_f32 v[54:55], v[94:95], v[128:129], v[54:55] op_sel_hi:[0,1,1]
	v_mov_b32_e32 v126, v125
	v_pk_fma_f32 v[54:55], v[94:95], v[126:127], v[54:55] op_sel:[1,0,0]
	ds_read2_b32 v[94:95], v0 offset0:2 offset1:3
	ds_read2_b32 v[96:97], v93 offset0:2 offset1:3
	ds_read2_b32 v[98:99], v93 offset0:67 offset1:68
	v_add_u32_e32 v0, 0x418, v93
	s_waitcnt lgkmcnt(1)
	v_mov_b32_e32 v100, v96
	s_waitcnt lgkmcnt(0)
	v_mov_b32_e32 v101, v98
	v_pk_fma_f32 v[70:71], v[94:95], v[100:101], v[70:71] op_sel_hi:[0,1,1]
	ds_read2_b32 v[100:101], v93 offset0:132 offset1:133
	ds_read2_b32 v[102:103], v93 offset0:197 offset1:198
	v_mov_b32_e32 v98, v97
	v_pk_fma_f32 v[70:71], v[94:95], v[98:99], v[70:71] op_sel:[1,0,0]
	s_waitcnt lgkmcnt(1)
	v_mov_b32_e32 v104, v100
	s_waitcnt lgkmcnt(0)
	v_mov_b32_e32 v105, v102
	v_pk_fma_f32 v[68:69], v[94:95], v[104:105], v[68:69] op_sel_hi:[0,1,1]
	ds_read2_b32 v[104:105], v0 offset1:1
	v_add_u32_e32 v0, 0x51c, v93
	ds_read2_b32 v[106:107], v0 offset1:1
	v_add_u32_e32 v0, 0x620, v93
	v_mov_b32_e32 v102, v101
	s_waitcnt lgkmcnt(1)
	v_mov_b32_e32 v108, v104
	v_pk_fma_f32 v[68:69], v[94:95], v[102:103], v[68:69] op_sel:[1,0,0]
	s_waitcnt lgkmcnt(0)
	v_mov_b32_e32 v109, v106
	v_pk_fma_f32 v[66:67], v[94:95], v[108:109], v[66:67] op_sel_hi:[0,1,1]
	ds_read2_b32 v[108:109], v0 offset1:1
	v_add_u32_e32 v0, 0x724, v93
	ds_read2_b32 v[110:111], v0 offset1:1
	v_add_u32_e32 v0, 0x828, v93
	v_mov_b32_e32 v106, v105
	s_waitcnt lgkmcnt(1)
	v_mov_b32_e32 v112, v108
	v_pk_fma_f32 v[66:67], v[94:95], v[106:107], v[66:67] op_sel:[1,0,0]
	s_waitcnt lgkmcnt(0)
	v_mov_b32_e32 v113, v110
	v_pk_fma_f32 v[62:63], v[94:95], v[112:113], v[62:63] op_sel_hi:[0,1,1]
	ds_read2_b32 v[112:113], v0 offset1:1
	v_add_u32_e32 v0, 0x92c, v93
	ds_read2_b32 v[114:115], v0 offset1:1
	v_add_u32_e32 v0, 0xa30, v93
	v_mov_b32_e32 v110, v109
	s_waitcnt lgkmcnt(1)
	v_mov_b32_e32 v116, v112
	v_pk_fma_f32 v[62:63], v[94:95], v[110:111], v[62:63] op_sel:[1,0,0]
	s_waitcnt lgkmcnt(0)
	v_mov_b32_e32 v117, v114
	v_pk_fma_f32 v[60:61], v[94:95], v[116:117], v[60:61] op_sel_hi:[0,1,1]
	ds_read2_b32 v[116:117], v0 offset1:1
	v_add_u32_e32 v0, 0xb34, v93
	ds_read2_b32 v[118:119], v0 offset1:1
	v_add_u32_e32 v0, 0xc38, v93
	v_mov_b32_e32 v114, v113
	s_waitcnt lgkmcnt(1)
	v_mov_b32_e32 v120, v116
	v_pk_fma_f32 v[60:61], v[94:95], v[114:115], v[60:61] op_sel:[1,0,0]
	s_waitcnt lgkmcnt(0)
	v_mov_b32_e32 v121, v118
	v_pk_fma_f32 v[58:59], v[94:95], v[120:121], v[58:59] op_sel_hi:[0,1,1]
	ds_read2_b32 v[120:121], v0 offset1:1
	v_add_u32_e32 v0, 0xd3c, v93
	ds_read2_b32 v[122:123], v0 offset1:1
	v_add_u32_e32 v0, 0xe40, v93
	v_mov_b32_e32 v118, v117
	s_waitcnt lgkmcnt(1)
	v_mov_b32_e32 v124, v120
	v_pk_fma_f32 v[58:59], v[94:95], v[118:119], v[58:59] op_sel:[1,0,0]
	s_waitcnt lgkmcnt(0)
	v_mov_b32_e32 v125, v122
	v_pk_fma_f32 v[56:57], v[94:95], v[124:125], v[56:57] op_sel_hi:[0,1,1]
	ds_read2_b32 v[124:125], v0 offset1:1
	v_add_u32_e32 v0, 0xf44, v93
	ds_read2_b32 v[126:127], v0 offset1:1
	v_mov_b32_e32 v122, v121
	v_pk_fma_f32 v[56:57], v[94:95], v[122:123], v[56:57] op_sel:[1,0,0]
	s_waitcnt lgkmcnt(1)
	v_mov_b32_e32 v128, v124
	s_waitcnt lgkmcnt(0)
	v_mov_b32_e32 v129, v126
	v_pk_fma_f32 v[54:55], v[94:95], v[128:129], v[54:55] op_sel_hi:[0,1,1]
	v_mov_b32_e32 v126, v125
	v_pk_fma_f32 v[54:55], v[94:95], v[126:127], v[54:55] op_sel:[1,0,0]
	s_cbranch_scc0 .LBB0_16
; __device__ __forceinline__ unsigned q8x4(float a, float b, float c, float d, float s) { return q8_(a, s) | (q8_(b, s) << 8) | (q8_(c, s) << 16) | (q8_(d, s) << 24); }
; #define IN(k) ((const float*)gptr(ldp(PT, k)))
; __global__ void __launch_bounds__(NWAVES * 64, 2) fwd(Args args) {
;     ...
;           for (int it = F.bx; it < NL * 8 * 16; it += F.G) { const int l = it >> 7, h = (it >> 4) & 7, kb = it & 15;
;             const float* Wl = w_in + (size_t)l * D * DIN + (size_t)(kb * 64) * DIN + h * 64; const float* wuk = IN(6) + (size_t)l * 128 * 512 + h * 64;
;             { float t8[8], u16[16];
; #pragma unroll
;               for (int j = 0; j < 8; ++j) { const int i = F.tid + 512 * j; t8[j] = Wl[(size_t)(i >> 6) * DIN + (i & 63)]; }
; #pragma unroll
;               for (int j = 0; j < 16; ++j) { const int i = F.tid + 512 * j; u16[j] = wuk[(size_t)(i >> 6) * 512 + (i & 63)]; }
; #pragma unroll
;               for (int j = 0; j < 8; ++j) { const int i = F.tid + 512 * j; wt[(i >> 6) * 65 + (i & 63)] = t8[j]; }
; #pragma unroll
;               for (int j = 0; j < 16; ++j) { const int i = F.tid + 512 * j; uk[(i >> 6) * 65 + (i & 63)] = u16[j]; } }
;             __syncthreads();
;             const int c = F.tid >> 2, kq = F.tid & 3; float a[16];
; #pragma unroll
;             for (int j = 0; j < 16; ++j) a[j] = 0.f;
;             for (int d = 0; d < 64; ++d) { const float wv = uk[c * 65 + d];
; #pragma unroll
;                 for (int j = 0; j < 16; ++j) a[j] += wv * wt[(kq * 16 + j) * 65 + d]; }
;             unsigned char* p = (unsigned char*)WinT + ((size_t)l * NP + PC_QLAT + h * 128 + c) * D + kb * 64 + kq * 16; const float sq = 0.125f * QS_WQL;
;             *(v4u*)p = (v4u){q8x4(a[0], a[1], a[2], a[3], sq), q8x4(a[4], a[5], a[6], a[7], sq), q8x4(a[8], a[9], a[10], a[11], sq), q8x4(a[12], a[13], a[14], a[15], sq)};
;             __syncthreads(); } }
	v_mul_f32_e32 v0, 0x4461c71c, v70
	v_mul_f32_e32 v70, 0x4461c71c, v71
	v_med3_f32 v70, v70, s5, v92
	v_mul_f32_e32 v68, 0x4461c71c, v68
	v_mul_f32_e32 v69, 0x4461c71c, v69
	v_med3_f32 v0, v0, s5, v92
	v_rndne_f32_e32 v70, v70
	v_med3_f32 v68, v68, s5, v92
	v_med3_f32 v69, v69, s5, v92
	v_rndne_f32_e32 v0, v0
	v_cvt_i32_f32_e32 v70, v70
	v_rndne_f32_e32 v68, v68
	v_rndne_f32_e32 v69, v69
	v_cvt_i32_f32_e32 v0, v0
	v_cvt_i32_f32_sdwa v68, v68 dst_sel:WORD_1 dst_unused:UNUSED_PAD src0_sel:DWORD
	v_cvt_i32_f32_e32 v69, v69
	v_lshlrev_b32_e32 v70, 8, v70
	v_and_b32_e32 v70, 0xff00, v70
	v_and_b32_e32 v68, 0xff0000, v68
	v_perm_b32 v0, v69, v0, s6
	v_or3_b32 v68, v0, v70, v68
	v_mul_f32_e32 v0, 0x4461c71c, v66
	v_mul_f32_e32 v66, 0x4461c71c, v67
	v_med3_f32 v66, v66, s5, v92
	v_mul_f32_e32 v62, 0x4461c71c, v62
	v_mul_f32_e32 v63, 0x4461c71c, v63
	v_med3_f32 v0, v0, s5, v92
	v_rndne_f32_e32 v66, v66
	v_med3_f32 v62, v62, s5, v92
	v_med3_f32 v63, v63, s5, v92
	v_rndne_f32_e32 v0, v0
	v_cvt_i32_f32_e32 v66, v66
	v_rndne_f32_e32 v62, v62
	v_rndne_f32_e32 v63, v63
	v_cvt_i32_f32_e32 v0, v0
	v_cvt_i32_f32_sdwa v62, v62 dst_sel:WORD_1 dst_unused:UNUSED_PAD src0_sel:DWORD
	v_cvt_i32_f32_e32 v63, v63
	v_lshlrev_b32_e32 v66, 8, v66
	v_and_b32_e32 v66, 0xff00, v66
	v_and_b32_e32 v62, 0xff0000, v62
	v_perm_b32 v0, v63, v0, s6
	v_or3_b32 v69, v0, v66, v62
	v_mul_f32_e32 v0, 0x4461c71c, v60
	v_mul_f32_e32 v60, 0x4461c71c, v61
	v_med3_f32 v60, v60, s5, v92
	v_mul_f32_e32 v58, 0x4461c71c, v58
	v_mul_f32_e32 v59, 0x4461c71c, v59
	v_med3_f32 v0, v0, s5, v92
	v_rndne_f32_e32 v60, v60
	v_med3_f32 v58, v58, s5, v92
	v_med3_f32 v59, v59, s5, v92
	v_rndne_f32_e32 v0, v0
	v_cvt_i32_f32_e32 v60, v60
	v_rndne_f32_e32 v58, v58
	v_rndne_f32_e32 v59, v59
	v_cvt_i32_f32_e32 v0, v0
	v_cvt_i32_f32_sdwa v58, v58 dst_sel:WORD_1 dst_unused:UNUSED_PAD src0_sel:DWORD
	v_cvt_i32_f32_e32 v59, v59
	v_lshlrev_b32_e32 v60, 8, v60
	v_and_b32_e32 v60, 0xff00, v60
	v_and_b32_e32 v58, 0xff0000, v58
	v_perm_b32 v0, v59, v0, s6
	v_or3_b32 v70, v0, v60, v58
	v_mul_f32_e32 v0, 0x4461c71c, v56
	v_mul_f32_e32 v56, 0x4461c71c, v57
	v_med3_f32 v56, v56, s5, v92
	v_mul_f32_e32 v54, 0x4461c71c, v54
	v_mul_f32_e32 v55, 0x4461c71c, v55
	v_med3_f32 v0, v0, s5, v92
	v_rndne_f32_e32 v56, v56
	v_med3_f32 v54, v54, s5, v92
	v_med3_f32 v55, v55, s5, v92
	s_lshl_b64 s[2:3], s[2:3], 13
	s_lshl_b32 s8, s8, 7
	v_rndne_f32_e32 v0, v0
	v_cvt_i32_f32_e32 v56, v56
	v_rndne_f32_e32 v54, v54
	v_rndne_f32_e32 v55, v55
	s_or_b32 s2, s2, s8
	v_cvt_i32_f32_e32 v0, v0
	v_cvt_i32_f32_sdwa v54, v54 dst_sel:WORD_1 dst_unused:UNUSED_PAD src0_sel:DWORD
	v_cvt_i32_f32_e32 v55, v55
	v_lshl_add_u64 v[94:95], s[2:3], 0, v[2:3]
	v_lshlrev_b64 v[94:95], 10, v[94:95]
	v_lshl_add_u64 v[94:95], s[64:65], 0, v[94:95]
	v_lshlrev_b32_e32 v56, 8, v56
	v_lshl_add_u64 v[94:95], v[94:95], 0, s[0:1]
	v_and_b32_e32 v56, 0xff00, v56
	v_and_b32_e32 v54, 0xff0000, v54
	v_perm_b32 v0, v55, v0, s6
	s_addk_i32 s7, 0x80
	v_lshl_add_u64 v[94:95], v[94:95], 0, v[4:5]
	v_or3_b32 v71, v0, v56, v54
	s_cmpk_gt_i32 s7, 0x1ff
	global_store_dwordx4 v[94:95], v[68:71], off
	s_barrier
	s_cbranch_scc0 .LBB0_15
